# plus post-projection row phase: operands of all row sections prefetched at row top, conv weights loaded once before the row loop
# baseline (speedup 1.0000x reference)
; __device__ __forceinline__ float bflo(unsigned w) { return __uint_as_float(w << 16); }
; __device__ __forceinline__ float bfhi(unsigned w) { return __uint_as_float(w & 0xffff0000u); }
; __device__ __forceinline__ void postproj_phase(CArgs& A, int l, int vcu, int G) {
;     int tid = threadIdx.x; asm volatile("" : "+v"(tid));
;     const int lane = tid & 63, wave = __builtin_amdgcn_readfirstlane(tid >> 6);
;     const bf16* P = (const bf16*)(A.ws + WS_PROJ);
;     bf16* CQN = (bf16*)(A.ws + WS_CQN); bf16* CKVN = (bf16*)(A.ws + WS_CKVN); bf16* CZ = (bf16*)(A.ws + WS_CZ); unsigned char* Kb = A.ws + WS_K;
;     const f32x2* cs = (const f32x2*)(A.ws + WS_CS);
;     const float* gq = A.in[I_GQ] + l * QL; const float* gkv = A.in[I_GKV] + l * KVL; const float* cw = A.in[I_CONVW] + (size_t)l * 3 * CW;
;     for (int t = vcu * NWAVES + wave; t < NT; t += G * NWAVES) {
;         const int b = t / SEQ, s = t % SEQ; const bf16* pr = P + (size_t)t * NINP;
;     ...
;         {
;             const int c0 = 16 * lane;
;             float z[3][16];
; #pragma unroll
;             for (int d = 0; d < 3; ++d) {
;                 const int ss = s + d - 1; const bool ok = (ss >= 0 && ss < SEQ);
;                 const bf16* p2 = pr + (ptrdiff_t)(d - 1) * NINP;
;                 u32x4 gc0 = {0, 0, 0, 0}, gc1 = gc0, u0 = gc0, u1 = gc0;
;                 if (ok) { gc0 = *(const u32x4*)(p2 + PC_GC + c0); gc1 = *(const u32x4*)(p2 + PC_GC + c0 + 8); u0 = *(const u32x4*)(p2 + PC_U + c0); u1 = *(const u32x4*)(p2 + PC_U + c0 + 8); }
;                 const unsigned gw_[8] = {gc0.x, gc0.y, gc0.z, gc0.w, gc1.x, gc1.y, gc1.z, gc1.w}, uw_[8] = {u0.x, u0.y, u0.z, u0.w, u1.x, u1.y, u1.z, u1.w};
; #pragma unroll
;                 for (int q = 0; q < 8; ++q) { z[d][2 * q] = bflo(gw_[q]) * bflo(uw_[q]); z[d][2 * q + 1] = bfhi(gw_[q]) * bfhi(uw_[q]); }
;             }
.LBB0_659:
	s_mov_b64 s[0:1], s[24:25]
	s_mov_b32 s0, s100
	s_waitcnt lgkmcnt(0)
	s_cmp_gt_i32 s0, 3
	s_cbranch_scc1 .LBB0_672
	s_mov_b64 s[0:1], s[24:25]
	s_mov_b32 s0, s101
	s_waitcnt lgkmcnt(0)
	s_cmp_lt_i32 s0, 4
	s_cbranch_scc1 .LBB0_671
	v_readlane_b32 s0, v255, 0
	v_readlane_b32 s1, v255, 1
	v_mov_b32_e32 v1, v0
	s_lshl_b32 s2, s97, 3
	v_readfirstlane_b32 s3, v1
	s_ashr_i32 s3, s3, 6
	s_add_i32 s6, s3, s2
	s_cmpk_gt_i32 s6, 0x1fff
	s_cbranch_scc1 .LBB0_671
	s_mov_b64 s[4:5], s[98:99]
	s_load_dwordx2 s[2:3], s[0:1], 0x38
	s_load_dwordx2 s[10:11], s[0:1], 0x48
	s_load_dwordx2 s[12:13], s[0:1], 0x60
	v_and_b32_e32 v6, 1, v1
	v_and_b32_e32 v8, 63, v1
	v_mov_b32_e32 v3, 0
	v_cmp_eq_u32_e64 s[0:1], 0, v6
	v_lshlrev_b32_e32 v6, 2, v1
	v_lshlrev_b32_e32 v2, 5, v8
	v_and_b32_e32 v54, 60, v6
	v_lshlrev_b32_e32 v6, 6, v8
	v_mov_b32_e32 v7, v3
	s_waitcnt lgkmcnt(0)
	s_add_u32 s8, s4, 0x200000
	v_lshl_add_u64 v[50:51], s[2:3], 0, v[2:3]
	v_lshl_add_u64 v[56:57], s[12:13], 0, v[6:7]
	s_mov_b64 s[2:3], 0x1000
	s_addc_u32 s9, s5, 0
	v_lshl_add_u64 v[58:59], v[56:57], 0, s[2:3]
	s_mov_b64 s[2:3], 0x2000
	s_ashr_i32 s7, s6, 31
	v_lshl_add_u64 v[60:61], v[56:57], 0, s[2:3]
	s_lshl_b64 s[2:3], s[6:7], 11
	v_lshlrev_b32_e32 v9, 3, v8
	v_or_b32_e32 v64, s2, v2
	v_mov_b32_e32 v65, s3
	s_lshl_b64 s[2:3], s[6:7], 9
	v_lshlrev_b32_e32 v4, 4, v8
	v_mov_b32_e32 v5, v3
	v_or_b32_e32 v66, s2, v9
	v_mov_b32_e32 v67, s3
	s_lshl_b64 s[2:3], s[6:7], 14
	v_lshl_add_u64 v[52:53], s[10:11], 0, v[4:5]
	v_mov_b32_e32 v55, v3
	v_or_b32_e32 v68, s2, v2
	v_or_b32_e32 v2, s2, v9
	v_mov_b32_e32 v3, s3
	s_mov_b64 s[10:11], 0x3e400400
	v_lshl_add_u64 v[70:71], v[2:3], 0, s[10:11]
	v_lshl_or_b32 v2, v8, 1, s2
	s_mov_b64 s[10:11], 0x3e400600
	v_mov_b32_e32 v69, s3
	v_lshl_add_u64 v[72:73], v[2:3], 0, s[10:11]
	v_or_b32_e32 v2, s2, v4
	s_mov_b64 s[2:3], 0x3e400000
	v_lshl_add_u64 v[74:75], v[2:3], 0, s[2:3]
	v_mbcnt_lo_u32_b32 v2, -1, 0
	v_mbcnt_hi_u32_b32 v97, -1, v2
	v_and_b32_e32 v2, 64, v97
	v_bfe_u32 v5, v1, 1, 5
	v_add_u32_e32 v99, 64, v2
	v_or_b32_e32 v2, v2, v54
	v_bfe_u32 v1, v1, 4, 2
	v_lshl_or_b32 v62, s6, 5, v5
	v_mov_b32_e32 v96, 0x358637bd
	s_mov_b32 s7, 0x800000
	s_mov_b32 s30, 0x46400000
	s_mov_b32 s31, 0x46c00000
	s_movk_i32 s33, 0xc0
	s_mov_b32 s34, 0x4b000000
	s_mov_b32 s35, 0x4b300000
	s_mov_b64 s[10:11], 0x3e3fd000
	s_mov_b64 s[12:13], 0x3e3fd800
	s_mov_b64 s[14:15], 0x3e401000
	s_mov_b64 s[16:17], 0x3e401800
	s_mov_b64 s[18:19], 0x3e405000
	s_mov_b64 s[20:21], 0x3e405800
	s_mov_b64 s[22:23], 0x3e400800
	s_mov_b32 s36, 0x3e400000
	s_mov_b32 s37, 0x47000000
	s_mov_b64 s[24:25], 0x400000
	s_mov_b64 s[26:27], 0x100000
	s_mov_b64 s[28:29], 0x2000000
	v_xor_b32_e32 v98, 1, v97
	v_lshlrev_b32_e32 v100, 2, v2
	v_mov_b64_e32 v[76:77], s[4:5]
	global_load_dwordx4 v[170:173], v[56:57], off offset:16
	global_load_dwordx4 v[174:177], v[56:57], off
	global_load_dwordx4 v[178:181], v[58:59], off offset:16
	global_load_dwordx4 v[182:185], v[58:59], off
	global_load_dwordx4 v[186:189], v[60:61], off offset:16
	global_load_dwordx4 v[190:193], v[60:61], off
	global_load_dwordx4 v[194:197], v[56:57], off offset:48
	global_load_dwordx4 v[198:201], v[56:57], off offset:32
	global_load_dwordx4 v[202:205], v[58:59], off offset:48
	global_load_dwordx4 v[206:209], v[58:59], off offset:32
	global_load_dwordx4 v[210:213], v[60:61], off offset:48
	global_load_dwordx4 v[214:217], v[60:61], off offset:32
	s_branch .LBB0_664
.LBB0_663:
	s_waitcnt vmcnt(3)
	v_lshlrev_b32_e32 v63, 16, v38
	s_waitcnt vmcnt(1)
	v_lshlrev_b32_e32 v80, 16, v46
	v_and_b32_e32 v38, 0xffff0000, v38
	v_and_b32_e32 v46, 0xffff0000, v46
	v_mul_f32_e32 v137, v38, v46
	v_lshlrev_b32_e32 v38, 16, v39
	v_lshlrev_b32_e32 v46, 16, v47
	v_mul_f32_e32 v95, v38, v46
	v_and_b32_e32 v38, 0xffff0000, v39
	v_and_b32_e32 v39, 0xffff0000, v47
	v_mul_f32_e32 v93, v38, v39
	v_lshlrev_b32_e32 v38, 16, v40
	v_lshlrev_b32_e32 v39, 16, v48
	v_mul_f32_e32 v91, v38, v39
	v_and_b32_e32 v38, 0xffff0000, v40
	v_and_b32_e32 v39, 0xffff0000, v48
	v_mul_f32_e32 v89, v38, v39
	v_lshlrev_b32_e32 v38, 16, v41
	v_lshlrev_b32_e32 v39, 16, v49
	v_mul_f32_e32 v87, v38, v39
	v_and_b32_e32 v38, 0xffff0000, v41
	v_and_b32_e32 v39, 0xffff0000, v49
	v_mul_f32_e32 v85, v38, v39
	v_lshlrev_b32_e32 v38, 16, v34
	s_waitcnt vmcnt(0)
; __device__ __forceinline__ float bflo(unsigned w) { return __uint_as_float(w << 16); }
; __device__ __forceinline__ float bfhi(unsigned w) { return __uint_as_float(w & 0xffff0000u); }
; __device__ __forceinline__ void postproj_phase(CArgs& A, int l, int vcu, int G) {
;     ...
;         {
;             const int c0 = 16 * lane;
;             float z[3][16];
; #pragma unroll
;             for (int d = 0; d < 3; ++d) {
;                 const int ss = s + d - 1; const bool ok = (ss >= 0 && ss < SEQ);
;                 const bf16* p2 = pr + (ptrdiff_t)(d - 1) * NINP;
;                 u32x4 gc0 = {0, 0, 0, 0}, gc1 = gc0, u0 = gc0, u1 = gc0;
;                 if (ok) { gc0 = *(const u32x4*)(p2 + PC_GC + c0); gc1 = *(const u32x4*)(p2 + PC_GC + c0 + 8); u0 = *(const u32x4*)(p2 + PC_U + c0); u1 = *(const u32x4*)(p2 + PC_U + c0 + 8); }
;                 const unsigned gw_[8] = {gc0.x, gc0.y, gc0.z, gc0.w, gc1.x, gc1.y, gc1.z, gc1.w}, uw_[8] = {u0.x, u0.y, u0.z, u0.w, u1.x, u1.y, u1.z, u1.w};
; #pragma unroll
;                 for (int q = 0; q < 8; ++q) { z[d][2 * q] = bflo(gw_[q]) * bflo(uw_[q]); z[d][2 * q + 1] = bfhi(gw_[q]) * bfhi(uw_[q]); }
;             }
;             const u32x4 gb0 = *(const u32x4*)(pr + PC_GB + c0), gb1 = *(const u32x4*)(pr + PC_GB + c0 + 8);
;             const unsigned gbw[8] = {gb0.x, gb0.y, gb0.z, gb0.w, gb1.x, gb1.y, gb1.z, gb1.w};
;             float o[16];
; #pragma unroll
;             for (int q4 = 0; q4 < 4; ++q4) { const f32x4 w0 = *(const f32x4*)(cw + c0 + 4 * q4), w1 = *(const f32x4*)(cw + CW + c0 + 4 * q4), w2 = *(const f32x4*)(cw + 2 * CW + c0 + 4 * q4);
; #pragma unroll
;                 for (int q = 0; q < 4; ++q) { const int i = 4 * q4 + q; const float gbv = (i & 1) ? bfhi(gbw[i >> 1]) : bflo(gbw[i >> 1]); o[i] = gbv * (w0[q] * z[0][i] + w1[q] * z[1][i] + w2[q] * z[2][i]); } }
	v_lshlrev_b32_e32 v39, 16, v42
	v_mul_f32_e32 v83, v38, v39
	v_and_b32_e32 v34, 0xffff0000, v34
	v_and_b32_e32 v38, 0xffff0000, v42
	v_mul_f32_e32 v81, v34, v38
	v_lshlrev_b32_e32 v34, 16, v35
	v_lshlrev_b32_e32 v38, 16, v43
	v_mul_f32_e32 v49, v34, v38
	v_and_b32_e32 v34, 0xffff0000, v35
	v_and_b32_e32 v35, 0xffff0000, v43
	v_mul_f32_e32 v47, v34, v35
	v_lshlrev_b32_e32 v34, 16, v36
	v_lshlrev_b32_e32 v35, 16, v44
	v_mul_f32_e32 v43, v34, v35
	v_and_b32_e32 v34, 0xffff0000, v36
	v_and_b32_e32 v35, 0xffff0000, v44
	v_mul_f32_e32 v41, v34, v35
	v_lshlrev_b32_e32 v34, 16, v37
	v_lshlrev_b32_e32 v35, 16, v45
	v_mul_f32_e32 v39, v34, v35
	v_and_b32_e32 v34, 0xffff0000, v37
	v_and_b32_e32 v35, 0xffff0000, v45
	v_mul_f32_e32 v35, v34, v35
	v_lshlrev_b32_e32 v34, 16, v10
	v_lshlrev_b32_e32 v36, 16, v14
	v_and_b32_e32 v10, 0xffff0000, v10
	v_and_b32_e32 v14, 0xffff0000, v14
	v_mul_f32_e32 v136, v10, v14
	v_lshlrev_b32_e32 v10, 16, v11
	v_lshlrev_b32_e32 v14, 16, v15
	v_mul_f32_e32 v94, v10, v14
	v_and_b32_e32 v10, 0xffff0000, v11
	v_and_b32_e32 v11, 0xffff0000, v15
	v_mul_f32_e32 v92, v10, v11
	v_lshlrev_b32_e32 v10, 16, v12
	v_lshlrev_b32_e32 v11, 16, v16
	v_mul_f32_e32 v90, v10, v11
	v_and_b32_e32 v10, 0xffff0000, v12
	v_and_b32_e32 v11, 0xffff0000, v16
	v_mul_f32_e32 v88, v10, v11
	v_lshlrev_b32_e32 v10, 16, v13
	v_lshlrev_b32_e32 v11, 16, v17
	v_mul_f32_e32 v134, v34, v36
	v_mul_f32_e32 v86, v10, v11
	v_and_b32_e32 v10, 0xffff0000, v13
	v_and_b32_e32 v11, 0xffff0000, v17
	v_add_co_u32_e32 v36, vcc, s36, v78
	v_mul_f32_e32 v84, v10, v11
	v_lshlrev_b32_e32 v10, 16, v2
	v_lshlrev_b32_e32 v11, 16, v6
	v_addc_co_u32_e32 v37, vcc, 0, v79, vcc
	v_mul_f32_e32 v82, v10, v11
	v_mov_b32_e32 v10, v160
	v_mov_b32_e32 v11, v161
	v_mov_b32_e32 v12, v162
	v_mov_b32_e32 v13, v163
	v_mov_b32_e32 v14, v170
	v_mov_b32_e32 v15, v171
	v_mov_b32_e32 v16, v172
	v_mov_b32_e32 v17, v173
	v_mov_b32_e32 v102, v174
	v_mov_b32_e32 v103, v175
	v_mov_b32_e32 v104, v176
	v_mov_b32_e32 v105, v177
	v_mov_b32_e32 v106, v178
	v_mov_b32_e32 v107, v179
	v_mov_b32_e32 v108, v180
	v_mov_b32_e32 v109, v181
	v_mov_b32_e32 v110, v182
	v_mov_b32_e32 v111, v183
	v_mov_b32_e32 v112, v184
	v_mov_b32_e32 v113, v185
	v_mov_b32_e32 v114, v186
	v_mov_b32_e32 v115, v187
	v_mov_b32_e32 v116, v188
	v_mov_b32_e32 v117, v189
	v_mov_b32_e32 v118, v190
	v_mov_b32_e32 v119, v191
	v_mov_b32_e32 v120, v192
	v_mov_b32_e32 v121, v193
	v_and_b32_e32 v2, 0xffff0000, v2
	v_and_b32_e32 v6, 0xffff0000, v6
	v_mul_f32_e32 v135, v63, v80
	v_mul_f32_e32 v80, v2, v6
	v_lshlrev_b32_e32 v2, 16, v3
	v_lshlrev_b32_e32 v6, 16, v7
	v_mul_f32_e32 v48, v2, v6
	v_and_b32_e32 v2, 0xffff0000, v3
	v_and_b32_e32 v3, 0xffff0000, v7
	v_mul_f32_e32 v46, v2, v3
	v_lshlrev_b32_e32 v2, 16, v4
	v_lshlrev_b32_e32 v3, 16, v8
	v_mul_f32_e32 v42, v2, v3
	v_and_b32_e32 v2, 0xffff0000, v4
	v_and_b32_e32 v3, 0xffff0000, v8
	v_mul_f32_e32 v40, v2, v3
	v_lshlrev_b32_e32 v2, 16, v5
	v_lshlrev_b32_e32 v3, 16, v9
	v_mul_f32_e32 v38, v2, v3
	v_and_b32_e32 v2, 0xffff0000, v5
	v_and_b32_e32 v3, 0xffff0000, v9
	v_mul_f32_e32 v34, v2, v3
	v_lshlrev_b32_e32 v2, 16, v30
	v_lshlrev_b32_e32 v3, 16, v26
	v_mul_f32_e32 v36, v2, v3
	v_and_b32_e32 v2, 0xffff0000, v30
	v_and_b32_e32 v3, 0xffff0000, v26
	v_mul_f32_e32 v37, v2, v3
	v_lshlrev_b32_e32 v2, 16, v27
	v_lshlrev_b32_e32 v3, 16, v31
	v_mul_f32_e32 v44, v3, v2
	v_and_b32_e32 v2, 0xffff0000, v31
	v_and_b32_e32 v3, 0xffff0000, v27
	v_mul_f32_e32 v45, v2, v3
	v_lshlrev_b32_e32 v2, 16, v32
	v_lshlrev_b32_e32 v3, 16, v28
	v_mul_f32_e32 v63, v2, v3
	v_and_b32_e32 v2, 0xffff0000, v32
	v_and_b32_e32 v3, 0xffff0000, v28
	v_mul_f32_e32 v101, v2, v3
	v_lshlrev_b32_e32 v2, 16, v29
	v_lshlrev_b32_e32 v3, 16, v33
	v_mul_f32_e32 v138, v3, v2
	v_and_b32_e32 v2, 0xffff0000, v33
	v_and_b32_e32 v3, 0xffff0000, v29
	v_lshl_add_u64 v[30:31], v[78:79], 0, s[22:23]
	v_mul_f32_e32 v139, v2, v3
	v_mov_b32_e32 v2, v166
	v_mov_b32_e32 v3, v167
	v_mov_b32_e32 v4, v168
	v_mov_b32_e32 v5, v169
	v_mov_b32_e32 v6, v194
	v_mov_b32_e32 v7, v195
	v_mov_b32_e32 v8, v196
	v_mov_b32_e32 v9, v197
	v_mov_b32_e32 v26, v198
	v_mov_b32_e32 v27, v199
	v_mov_b32_e32 v28, v200
	v_mov_b32_e32 v29, v201
	s_nop 0
	v_mov_b32_e32 v30, v202
	v_mov_b32_e32 v31, v203
	v_mov_b32_e32 v32, v204
	v_mov_b32_e32 v33, v205
	v_mov_b32_e32 v122, v206
	v_mov_b32_e32 v123, v207
	v_mov_b32_e32 v124, v208
	v_mov_b32_e32 v125, v209
	v_mov_b32_e32 v126, v210
	v_mov_b32_e32 v127, v211
	v_mov_b32_e32 v128, v212
	v_mov_b32_e32 v129, v213
	v_mov_b32_e32 v130, v214
	v_mov_b32_e32 v131, v215
	v_mov_b32_e32 v132, v216
	v_mov_b32_e32 v133, v217
	v_lshlrev_b32_e32 v140, 16, v22
	v_lshlrev_b32_e32 v78, 16, v18
	v_and_b32_e32 v22, 0xffff0000, v22
	v_and_b32_e32 v18, 0xffff0000, v18
	v_mul_f32_e32 v22, v22, v18
	v_lshlrev_b32_e32 v18, 16, v19
	v_lshlrev_b32_e32 v79, 16, v23
	v_mul_f32_e32 v79, v79, v18
	v_and_b32_e32 v18, 0xffff0000, v23
	v_and_b32_e32 v19, 0xffff0000, v19
	v_mul_f32_e32 v23, v18, v19
	v_lshlrev_b32_e32 v18, 16, v24
	v_lshlrev_b32_e32 v19, 16, v20
	v_mul_f32_e32 v78, v140, v78
	v_mul_f32_e32 v140, v18, v19
	v_and_b32_e32 v18, 0xffff0000, v24
	v_and_b32_e32 v19, 0xffff0000, v20
	v_mul_f32_e32 v20, v18, v19
	v_lshlrev_b32_e32 v18, 16, v21
	v_lshlrev_b32_e32 v19, 16, v25
	v_mul_f32_e32 v24, v19, v18
	v_and_b32_e32 v18, 0xffff0000, v25
	v_and_b32_e32 v19, 0xffff0000, v21
	v_mul_f32_e32 v21, v18, v19
	s_add_i32 s2, s6, 0x800
	s_waitcnt vmcnt(13)
	v_lshlrev_b32_e32 v25, 16, v10
	v_and_b32_e32 v10, 0xffff0000, v10
	s_waitcnt vmcnt(11)
	v_mov_b32_e32 v18, v102
	v_add_u32_e32 v62, 0x10000, v62
	s_waitcnt vmcnt(9)
; __device__ __forceinline__ unsigned cvtpk(float lo, float hi) { unsigned r; asm volatile("v_cvt_pk_bf16_f32 %0, %1, %2" : "=v"(r) : "v"(lo), "v"(hi)); return r; }
; __device__ __forceinline__ float bflo(unsigned w) { return __uint_as_float(w << 16); }
; __device__ __forceinline__ float bfhi(unsigned w) { return __uint_as_float(w & 0xffff0000u); }
; __device__ __forceinline__ void postproj_phase(CArgs& A, int l, int vcu, int G) {
;     ...
;     for (int t = vcu * NWAVES + wave; t < NT; t += G * NWAVES) {
;         const int b = t / SEQ, s = t % SEQ; const bf16* pr = P + (size_t)t * NINP;
;         {
;             const u32x4 w = *(const u32x4*)(pr + PC_CQ + 8 * lane); float v[8] = {bflo(w.x), bfhi(w.x), bflo(w.y), bfhi(w.y), bflo(w.z), bfhi(w.z), bflo(w.w), bfhi(w.w)};
;     ...
;             const u32x4 gb0 = *(const u32x4*)(pr + PC_GB + c0), gb1 = *(const u32x4*)(pr + PC_GB + c0 + 8);
;             const unsigned gbw[8] = {gb0.x, gb0.y, gb0.z, gb0.w, gb1.x, gb1.y, gb1.z, gb1.w};
;             float o[16];
; #pragma unroll
;             for (int q4 = 0; q4 < 4; ++q4) { const f32x4 w0 = *(const f32x4*)(cw + c0 + 4 * q4), w1 = *(const f32x4*)(cw + CW + c0 + 4 * q4), w2 = *(const f32x4*)(cw + 2 * CW + c0 + 4 * q4);
; #pragma unroll
;                 for (int q = 0; q < 4; ++q) { const int i = 4 * q4 + q; const float gbv = (i & 1) ? bfhi(gbw[i >> 1]) : bflo(gbw[i >> 1]); o[i] = gbv * (w0[q] * z[0][i] + w1[q] * z[1][i] + w2[q] * z[2][i]); } }
;             u32x4 o0, o1; o0.x = cvtpk(o[0], o[1]); o0.y = cvtpk(o[2], o[3]); o0.z = cvtpk(o[4], o[5]); o0.w = cvtpk(o[6], o[7]); o1.x = cvtpk(o[8], o[9]); o1.y = cvtpk(o[10], o[11]); o1.z = cvtpk(o[12], o[13]); o1.w = cvtpk(o[14], o[15]);
;             *(u32x4*)(CZ + (size_t)t * CW + c0) = o0; *(u32x4*)(CZ + (size_t)t * CW + c0 + 8) = o1;
	v_mov_b32_e32 v19, v110
	v_pk_mul_f32 v[18:19], v[134:135], v[18:19]
	v_mov_b32_e32 v110, v103
	v_add_f32_e32 v18, v18, v19
	s_waitcnt vmcnt(7)
	v_fmac_f32_e32 v18, v36, v118
	v_mul_f32_e32 v25, v18, v25
	v_pk_mul_f32 v[18:19], v[136:137], v[110:111]
	v_lshl_add_u64 v[66:67], v[66:67], 0, s[26:27]
	v_add_f32_e32 v18, v18, v19
	v_fmac_f32_e32 v18, v37, v119
	v_mul_f32_e32 v36, v18, v10
	v_mov_b32_e32 v18, v104
	v_mov_b32_e32 v19, v112
	v_pk_mul_f32 v[18:19], v[94:95], v[18:19]
	v_lshlrev_b32_e32 v10, 16, v11
	v_add_f32_e32 v18, v18, v19
	v_fmac_f32_e32 v18, v44, v120
	v_mov_b32_e32 v112, v105
	v_mul_f32_e32 v18, v18, v10
	v_and_b32_e32 v19, 0xffff0000, v11
	v_pk_mul_f32 v[10:11], v[92:93], v[112:113]
	v_lshlrev_b32_e32 v37, 16, v12
	v_add_f32_e32 v10, v10, v11
	v_fmac_f32_e32 v10, v45, v121
	v_mul_f32_e32 v19, v10, v19
	v_mov_b32_e32 v10, v14
	v_mov_b32_e32 v11, v106
	v_pk_mul_f32 v[10:11], v[90:91], v[10:11]
	v_mov_b32_e32 v106, v15
	v_add_f32_e32 v10, v10, v11
	v_fmac_f32_e32 v10, v63, v114
	v_mul_f32_e32 v14, v10, v37
	v_pk_mul_f32 v[10:11], v[88:89], v[106:107]
	v_and_b32_e32 v12, 0xffff0000, v12
	v_add_f32_e32 v10, v10, v11
	v_fmac_f32_e32 v10, v101, v115
	v_mul_f32_e32 v12, v10, v12
	v_mov_b32_e32 v10, v16
	v_mov_b32_e32 v11, v108
	v_pk_mul_f32 v[10:11], v[86:87], v[10:11]
	v_lshlrev_b32_e32 v15, 16, v13
	v_add_f32_e32 v10, v10, v11
	v_fmac_f32_e32 v10, v138, v116
	v_mov_b32_e32 v108, v17
	v_mul_f32_e32 v15, v10, v15
	v_pk_mul_f32 v[10:11], v[84:85], v[108:109]
	v_and_b32_e32 v13, 0xffff0000, v13
	v_add_f32_e32 v10, v10, v11
	v_fmac_f32_e32 v10, v139, v117
	v_mul_f32_e32 v13, v10, v13
	s_waitcnt vmcnt(4)
	v_mov_b32_e32 v10, v26
	s_waitcnt vmcnt(2)
	v_mov_b32_e32 v11, v122
	v_pk_mul_f32 v[10:11], v[82:83], v[10:11]
	v_lshlrev_b32_e32 v16, 16, v2
	v_add_f32_e32 v10, v10, v11
	s_waitcnt vmcnt(0)
	v_fmac_f32_e32 v10, v78, v130
	v_mov_b32_e32 v122, v27
	v_mul_f32_e32 v16, v10, v16
	v_pk_mul_f32 v[10:11], v[80:81], v[122:123]
	v_and_b32_e32 v2, 0xffff0000, v2
	v_add_f32_e32 v10, v10, v11
	v_fmac_f32_e32 v10, v22, v131
	v_mul_f32_e32 v17, v10, v2
	v_mov_b32_e32 v10, v28
	v_mov_b32_e32 v11, v124
	v_pk_mul_f32 v[10:11], v[48:49], v[10:11]
	v_lshlrev_b32_e32 v2, 16, v3
	v_add_f32_e32 v10, v10, v11
	v_fmac_f32_e32 v10, v79, v132
	v_mov_b32_e32 v124, v29
	v_mul_f32_e32 v10, v10, v2
	v_and_b32_e32 v11, 0xffff0000, v3
	v_pk_mul_f32 v[2:3], v[46:47], v[124:125]
	v_lshlrev_b32_e32 v22, 16, v4
	v_add_f32_e32 v2, v2, v3
	v_fmac_f32_e32 v2, v23, v133
	v_mul_f32_e32 v11, v2, v11
	v_mov_b32_e32 v2, v6
	v_mov_b32_e32 v3, v30
	v_pk_mul_f32 v[2:3], v[42:43], v[2:3]
	v_mov_b32_e32 v30, v7
	v_add_f32_e32 v2, v2, v3
	v_fmac_f32_e32 v2, v140, v126
	v_mul_f32_e32 v22, v2, v22
	v_pk_mul_f32 v[2:3], v[40:41], v[30:31]
	v_and_b32_e32 v4, 0xffff0000, v4
	v_add_f32_e32 v2, v2, v3
	v_fmac_f32_e32 v2, v20, v127
	v_mul_f32_e32 v20, v2, v4
	v_mov_b32_e32 v2, v8
	v_mov_b32_e32 v3, v32
	v_pk_mul_f32 v[2:3], v[38:39], v[2:3]
	v_lshlrev_b32_e32 v4, 16, v5
	v_add_f32_e32 v2, v2, v3
	v_fmac_f32_e32 v2, v24, v128
	v_mov_b32_e32 v32, v9
	v_mul_f32_e32 v23, v2, v4
	v_pk_mul_f32 v[2:3], v[34:35], v[32:33]
	v_and_b32_e32 v4, 0xffff0000, v5
	v_add_f32_e32 v2, v2, v3
	v_fmac_f32_e32 v2, v21, v129
	v_mul_f32_e32 v9, v2, v4
	v_cvt_pk_bf16_f32 v2, v25, v36
	v_cvt_pk_bf16_f32 v3, v18, v19
	v_cvt_pk_bf16_f32 v4, v14, v12
	v_cvt_pk_bf16_f32 v5, v15, v13
	v_cvt_pk_bf16_f32 v6, v16, v17
	v_cvt_pk_bf16_f32 v7, v10, v11
	v_lshl_add_u64 v[10:11], s[4:5], 0, v[64:65]
	v_add_co_u32_e32 v10, vcc, s37, v10
	v_lshl_add_u64 v[64:65], v[64:65], 0, s[24:25]
	s_nop 0
	v_addc_co_u32_e32 v11, vcc, 0, v11, vcc
	v_lshl_add_u64 v[68:69], v[68:69], 0, s[28:29]
	v_lshl_add_u64 v[70:71], v[70:71], 0, s[28:29]
	v_lshl_add_u64 v[72:73], v[72:73], 0, s[28:29]
	v_lshl_add_u64 v[74:75], v[74:75], 0, s[28:29]
	s_cmpk_lt_i32 s6, 0x1800
	s_mov_b32 s6, s2
	v_cvt_pk_bf16_f32 v8, v22, v20
	v_cvt_pk_bf16_f32 v9, v23, v9
	global_store_dwordx4 v[10:11], v[2:5], off
	global_store_dwordx4 v[10:11], v[6:9], off offset:16
	s_cbranch_scc0 .LBB0_671
.LBB0_664:
	v_lshl_add_u64 v[14:15], s[4:5], 0, v[74:75]
	global_load_dwordx4 v[2:5], v[14:15], off
	global_load_dwordx4 v[6:9], v[50:51], off
	global_load_dwordx4 v[10:13], v[50:51], off offset:16
	v_mov_b32_e32 v14, 0
	v_mov_b32_e32 v15, 0
	v_lshl_add_u64 v[16:17], s[4:5], 0, v[66:67]
	v_lshl_add_u64 v[18:19], s[4:5], 0, v[70:71]
	v_ashrrev_i32_e32 v63, 31, v62
	v_lshl_add_u64 v[78:79], s[4:5], 0, v[68:69]
	global_load_dwordx2 v[142:143], v[18:19], off
	global_load_dwordx4 v[144:147], v[52:53], off
	v_lshl_add_u64 v[148:149], s[4:5], 0, v[72:73]
	global_load_ushort v150, v[148:149], off
	v_lshl_add_u64 v[152:153], v[62:63], 3, s[8:9]
	global_load_dwordx2 v[154:155], v[152:153], off
	v_mov_b32_e32 v158, s36
	v_mov_b32_e32 v159, 0
	v_lshl_add_u64 v[156:157], v[78:79], 0, v[158:159]
	global_load_dwordx4 v[160:163], v[156:157], off offset:2048
	v_lshl_add_u64 v[164:165], v[78:79], 0, s[22:23]
	global_load_dwordx4 v[166:169], v[164:165], off offset:16
	s_waitcnt vmcnt(0)
; __device__ __forceinline__ void postproj_phase(CArgs& A, int l, int vcu, int G) {
;     ...
;         {
;             const u32x4 w = *(const u32x4*)(pr + PC_CQ + 8 * lane); float v[8] = {bflo(w.x), bfhi(w.x), bflo(w.y), bfhi(w.y), bflo(w.z), bfhi(w.z), bflo(w.w), bfhi(w.w)};
;             float ss = 0.f;
; #pragma unroll
;             for (int q = 0; q < 8; ++q) ss += v[q] * v[q];
;             const float rstd = rsqrtf(wave_sum(ss) * (1.0f / QL) + EPS);
;             const f32x4 g0 = *(const f32x4*)(gq + 8 * lane), g1 = *(const f32x4*)(gq + 8 * lane + 4);
;             u32x4 o; o.x = cvtpk(v[0] * rstd * g0.x, v[1] * rstd * g0.y); o.y = cvtpk(v[2] * rstd * g0.z, v[3] * rstd * g0.w); o.z = cvtpk(v[4] * rstd * g1.x, v[5] * rstd * g1.y); o.w = cvtpk(v[6] * rstd * g1.z, v[7] * rstd * g1.w);
;             *(u32x2*)((unsigned char*)CQN + (size_t)t * QL + 8 * lane) = pack8_fp8((f32x4){v[0] * rstd * g0.x, v[1] * rstd * g0.y, v[2] * rstd * g0.z, v[3] * rstd * g0.w}, (f32x4){v[4] * rstd * g1.x, v[5] * rstd * g1.y, v[6] * rstd * g1.z, v[7] * rstd * g1.w});
;         }
;         {
;             const u32x2 w = *(const u32x2*)(pr + PC_CKV + 4 * lane); float v[4] = {bflo(w.x), bfhi(w.x), bflo(w.y), bfhi(w.y)};
;             const float rstd = rsqrtf(wave_sum(v[0] * v[0] + v[1] * v[1] + v[2] * v[2] + v[3] * v[3]) * (1.0f / KVL) + EPS);
;             const f32x4 g0 = *(const f32x4*)(gkv + 4 * lane);
;             u32x2 o; o.x = cvtpk(v[0] * rstd * g0.x, v[1] * rstd * g0.y); o.y = cvtpk(v[2] * rstd * g0.z, v[3] * rstd * g0.w);
;             *(u32x2*)(CKVN + (size_t)t * KVL + 4 * lane) = o;
;         }
;         {
;             const float v = __uint_as_float((unsigned)pr[PC_KPE + lane] << 16); const float o = __shfl_xor(v, 1);
;             const f32x2 c = cs[t * 32 + (lane >> 1)];
;             const float r = ((lane & 1) ? (v * c.x + o * c.y) : (v * c.x - o * c.y)) * 0.25f;
;             const int w1 = __builtin_amdgcn_cvt_pk_fp8_f32(r, r, 0, false) & 0xff;
;             const unsigned q0 = (unsigned)__builtin_amdgcn_update_dpp(0, w1, 0x00, 0xf, 0xf, true), q1 = (unsigned)__builtin_amdgcn_update_dpp(0, w1, 0x55, 0xf, 0xf, true);
;             const unsigned q2 = (unsigned)__builtin_amdgcn_update_dpp(0, w1, 0xAA, 0xf, 0xf, true), q3 = (unsigned)__builtin_amdgcn_update_dpp(0, w1, 0xFF, 0xf, 0xf, true);
;             const unsigned wq = q0 | (q1 << 8) | (q2 << 16) | (q3 << 24);
	v_and_b32_e32 v29, 0xffff0000, v2
	v_lshlrev_b32_e32 v28, 16, v2
	v_and_b32_e32 v2, 0xffff0000, v3
	v_lshlrev_b32_e32 v3, 16, v3
	v_mul_f32_e32 v30, v29, v29
	v_pk_mul_f32 v[22:23], v[2:3], v[2:3]
	v_fmac_f32_e32 v30, v28, v28
	v_and_b32_e32 v20, 0xffff0000, v4
	v_lshlrev_b32_e32 v21, 16, v4
	v_add_f32_e32 v23, v23, v30
	v_pk_mul_f32 v[24:25], v[20:21], v[20:21]
	v_add_f32_e32 v22, v22, v23
	v_and_b32_e32 v4, 0xffff0000, v5
	v_lshlrev_b32_e32 v5, 16, v5
	v_add_f32_e32 v22, v25, v22
	v_pk_mul_f32 v[26:27], v[4:5], v[4:5]
	v_add_f32_e32 v22, v24, v22
	v_add_f32_e32 v22, v27, v22
	v_add_f32_e32 v22, v26, v22
	s_nop 1
	v_add_f32_dpp v22, v22, v22 quad_perm:[1,0,3,2] row_mask:0xf bank_mask:0xf bound_ctrl:1
	s_nop 1
	v_add_f32_dpp v22, v22, v22 quad_perm:[2,3,0,1] row_mask:0xf bank_mask:0xf bound_ctrl:1
	s_nop 1
	v_add_f32_dpp v22, v22, v22 row_half_mirror row_mask:0xf bank_mask:0xf bound_ctrl:1
	s_nop 1
	v_add_f32_dpp v22, v22, v22 row_mirror row_mask:0xf bank_mask:0xf bound_ctrl:1
	s_nop 0
	v_readlane_b32 s38, v22, 16
	v_readlane_b32 s39, v22, 48
	v_readlane_b32 s2, v22, 0
	v_readlane_b32 s3, v22, 32
	v_mov_b32_e32 v22, s38
	v_mov_b32_e32 v23, s39
	v_pk_add_f32 v[22:23], s[2:3], v[22:23]
	s_nop 0
	v_add_f32_e32 v22, v22, v23
	v_fmamk_f32 v22, v22, 0x3b000000, v96
	v_mul_f32_e32 v23, 0x4b800000, v22
	v_cmp_gt_f32_e32 vcc, s7, v22
	s_nop 1
	v_cndmask_b32_e32 v22, v22, v23, vcc
	v_rsq_f32_e32 v24, v22
	v_add_co_u32_e64 v22, s[2:3], s30, v16
	v_mul_f32_e32 v25, 0x45800000, v24
	v_cndmask_b32_e32 v24, v24, v25, vcc
	v_mul_f32_e32 v25, v24, v28
	v_mul_f32_e32 v26, v24, v29
	v_mul_f32_e32 v3, v24, v3
	v_mul_f32_e32 v2, v24, v2
	v_mul_f32_e32 v21, v24, v21
	v_mul_f32_e32 v20, v24, v20
	v_mul_f32_e32 v6, v6, v25
	v_mul_f32_e32 v7, v7, v26
	v_mul_f32_e32 v3, v8, v3
	v_mul_f32_e32 v2, v9, v2
	v_mul_f32_e32 v8, v10, v21
	v_mul_f32_e32 v9, v11, v20
	v_cvt_pk_fp8_f32 v14, v6, v7
	v_cvt_pk_fp8_f32 v15, v8, v9
	v_mul_f32_e32 v5, v24, v5
	v_mul_f32_e32 v4, v24, v4
	v_mul_f32_e32 v5, v12, v5
	v_mul_f32_e32 v4, v13, v4
	v_cvt_pk_fp8_f32 v14, v3, v2 op_sel:[0,0,1]
	v_cvt_pk_fp8_f32 v15, v5, v4 op_sel:[0,0,1]
	v_addc_co_u32_e64 v23, s[2:3], 0, v17, s[2:3]
	v_cvt_pk_bf16_f32 v6, v6, v7
	v_cvt_pk_bf16_f32 v2, v3, v2
	v_mov_b32_e32 v28, 0
	v_cvt_pk_bf16_f32 v2, v8, v9
	v_lshl_add_u64 v[8:9], s[4:5], 0, v[72:73]
	v_cvt_pk_bf16_f32 v2, v5, v4
	global_store_dwordx2 v[22:23], v[14:15], off
	v_mov_b32_e32 v6, v142
	v_mov_b32_e32 v7, v143
	v_mov_b32_e32 v2, v144
	v_mov_b32_e32 v3, v145
	v_mov_b32_e32 v4, v146
	v_mov_b32_e32 v5, v147
	v_lshlrev_b32_e32 v10, 16, v6
	v_and_b32_e32 v11, 0xffff0000, v6
	v_and_b32_e32 v6, 0xffff0000, v7
	v_lshlrev_b32_e32 v7, 16, v7
	v_pk_mul_f32 v[12:13], v[10:11], v[10:11]
	v_pk_mul_f32 v[14:15], v[6:7], v[6:7]
	v_add_f32_e32 v12, v12, v13
	v_add_f32_e32 v12, v15, v12
	v_add_f32_e32 v12, v14, v12
	s_nop 1
	v_add_f32_dpp v12, v12, v12 quad_perm:[1,0,3,2] row_mask:0xf bank_mask:0xf bound_ctrl:1
	s_nop 1
	v_add_f32_dpp v12, v12, v12 quad_perm:[2,3,0,1] row_mask:0xf bank_mask:0xf bound_ctrl:1
	s_nop 1
	v_add_f32_dpp v12, v12, v12 row_half_mirror row_mask:0xf bank_mask:0xf bound_ctrl:1
	s_nop 1
	v_add_f32_dpp v12, v12, v12 row_mirror row_mask:0xf bank_mask:0xf bound_ctrl:1
	s_nop 0
	v_readlane_b32 s38, v12, 16
	v_readlane_b32 s39, v12, 48
	v_readlane_b32 s2, v12, 0
	v_readlane_b32 s3, v12, 32
	v_mov_b32_e32 v12, s38
	v_mov_b32_e32 v13, s39
	v_pk_add_f32 v[12:13], s[2:3], v[12:13]
	s_nop 0
	v_add_f32_e32 v12, v12, v13
	v_fmamk_f32 v12, v12, 0x3b800000, v96
	v_mul_f32_e32 v13, 0x4b800000, v12
	v_cmp_gt_f32_e32 vcc, s7, v12
	s_nop 1
	v_cndmask_b32_e32 v12, v12, v13, vcc
	v_rsq_f32_e32 v14, v12
	v_add_co_u32_e64 v12, s[2:3], s31, v16
	v_mov_b32_e32 v16, 0
	v_mul_f32_e32 v15, 0x45800000, v14
	v_cndmask_b32_e32 v14, v14, v15, vcc
	v_mul_f32_e32 v10, v14, v10
	v_mul_f32_e32 v11, v14, v11
	v_addc_co_u32_e64 v13, s[2:3], 0, v17, s[2:3]
	v_mul_f32_e32 v7, v14, v7
	v_mul_f32_e32 v6, v14, v6
	v_mul_f32_e32 v2, v2, v10
	v_mul_f32_e32 v3, v3, v11
	v_mul_f32_e32 v4, v4, v7
	v_mul_f32_e32 v5, v5, v6
	v_cvt_pk_bf16_f32 v2, v2, v3
	v_cvt_pk_bf16_f32 v3, v4, v5
	global_store_dwordx2 v[12:13], v[2:3], off
	v_mov_b32_e32 v9, v150
	v_lshl_add_u64 v[2:3], v[62:63], 3, s[8:9]
	v_mov_b32_e32 v18, v154
	v_mov_b32_e32 v19, v155
	v_cmp_lt_i32_e32 vcc, v98, v99
	s_ashr_i32 s2, s6, 31
	s_lshr_b32 s2, s2, 20
	v_cndmask_b32_e32 v20, v97, v98, vcc
	v_lshlrev_b32_e32 v25, 2, v20
	s_add_i32 s2, s6, s2
	s_ashr_i32 s3, s2, 12
	s_and_b32 s2, s2, 0xfffff000
	v_lshl_or_b32 v20, s3, 4, v1
	s_sub_i32 s2, s6, s2
	v_ashrrev_i32_e32 v21, 31, v20
	s_ashr_i32 s3, s2, 31
	v_lshlrev_b64 v[20:21], 12, v[20:21]
	s_add_i32 s38, s2, -1
	v_lshl_add_u64 v[20:21], v[20:21], 0, s[2:3]
	s_cmpk_gt_u32 s38, 0xfff
	v_mad_u64_u32 v[22:23], s[38:39], v20, s33, v[76:77]
	v_mad_i32_i24 v23, v21, s33, v23
	v_lshl_add_u64 v[20:21], v[22:23], 0, v[54:55]
	v_add_co_u32_e32 v22, vcc, s34, v20
	v_mov_b32_e32 v10, 0
	s_nop 0
	v_addc_co_u32_e32 v23, vcc, 0, v21, vcc
	v_add_co_u32_e32 v24, vcc, s35, v20
	v_mov_b32_e32 v11, 0
	v_mov_b32_e32 v12, 0
	v_mov_b32_e32 v13, 0
	v_mov_b32_e32 v2, 0
	v_mov_b32_e32 v3, 0
	v_mov_b32_e32 v4, 0
	v_mov_b32_e32 v5, 0
	v_mov_b32_e32 v14, 0
	v_mov_b32_e32 v15, 0
	v_mov_b32_e32 v17, 0
	v_mov_b32_e32 v6, 0
	v_mov_b32_e32 v7, 0
	v_mov_b32_e32 v8, 0
	v_lshlrev_b32_e32 v9, 16, v9
	ds_bpermute_b32 v27, v25, v9
	v_addc_co_u32_e32 v25, vcc, 0, v21, vcc
	v_add_co_u32_e32 v26, vcc, 0x4b600000, v20
	s_waitcnt lgkmcnt(0)
	v_mul_f32_e32 v19, v19, v27
	v_cndmask_b32_e64 v19, v19, -v19, s[0:1]
	v_fmac_f32_e32 v19, v18, v9
	v_mul_f32_e32 v9, 0x3e800000, v19
	v_cvt_pk_fp8_f32 v28, v9, v9
	v_addc_co_u32_e32 v27, vcc, 0, v21, vcc
	v_and_b32_e32 v9, 0xff, v28
	s_nop 1
	v_mov_b32_dpp v18, v9 quad_perm:[0,0,0,0] row_mask:0xf bank_mask:0xf bound_ctrl:1
	v_mov_b32_dpp v19, v9 quad_perm:[1,1,1,1] row_mask:0xf bank_mask:0xf bound_ctrl:1
	v_mov_b32_dpp v28, v9 quad_perm:[2,2,2,2] row_mask:0xf bank_mask:0xf bound_ctrl:1
	v_mov_b32_dpp v9, v9 quad_perm:[3,3,3,3] row_mask:0xf bank_mask:0xf bound_ctrl:1
	v_lshl_or_b32 v18, v19, 8, v18
	v_lshlrev_b32_e32 v19, 16, v28
	v_lshlrev_b32_e32 v9, 24, v9
	v_or3_b32 v9, v18, v19, v9
	ds_bpermute_b32 v9, v100, v9
	v_add_co_u32_e32 v18, vcc, 0x4b900000, v20
	s_nop 1
	v_addc_co_u32_e32 v19, vcc, 0, v21, vcc
	s_waitcnt lgkmcnt(0)
	global_store_dword v[22:23], v9, off offset:128
	global_store_dword v[24:25], v9, off offset:128
	global_store_dword v[26:27], v9, off offset:128
	global_store_dword v[18:19], v9, off offset:128
	v_mov_b32_e32 v9, 0
	s_cbranch_scc1 .LBB0_666
	v_add_co_u32_e32 v18, vcc, 0x3e3fd000, v78
	v_lshl_add_u64 v[6:7], v[78:79], 0, s[10:11]
	s_nop 0
	v_addc_co_u32_e32 v19, vcc, 0, v79, vcc
	global_load_dwordx4 v[10:13], v[18:19], off
	global_load_dwordx4 v[2:5], v[6:7], off offset:16
	v_lshl_add_u64 v[20:21], v[78:79], 0, s[12:13]
	global_load_dwordx4 v[14:17], v[18:19], off offset:2048
	global_load_dwordx4 v[6:9], v[20:21], off offset:16

; __device__ __forceinline__ void postproj_phase(CArgs& A, int l, int vcu, int G) {
;     int tid = threadIdx.x; asm volatile("" : "+v"(tid));
;     const int lane = tid & 63, wave = __builtin_amdgcn_readfirstlane(tid >> 6);
;     const bf16* P = (const bf16*)(A.ws + WS_PROJ);
;     bf16* CQN = (bf16*)(A.ws + WS_CQN); bf16* CKVN = (bf16*)(A.ws + WS_CKVN); bf16* CZ = (bf16*)(A.ws + WS_CZ); unsigned char* Kb = A.ws + WS_K;
;     const f32x2* cs = (const f32x2*)(A.ws + WS_CS);
;     const float* gq = A.in[I_GQ] + l * QL; const float* gkv = A.in[I_GKV] + l * KVL; const float* cw = A.in[I_CONVW] + (size_t)l * 3 * CW;
;     for (int t = vcu * NWAVES + wave; t < NT; t += G * NWAVES) {
;         const int b = t / SEQ, s = t % SEQ; const bf16* pr = P + (size_t)t * NINP;
.LBB0_1922:
	s_mov_b64 s[0:1], s[24:25]
	s_mov_b32 s0, s100
	s_waitcnt lgkmcnt(0)
	s_cmp_gt_i32 s0, 13
	s_cbranch_scc1 .LBB0_1935
	s_mov_b64 s[0:1], s[24:25]
	s_mov_b32 s0, s101
	s_waitcnt lgkmcnt(0)
	s_cmp_lt_i32 s0, 14
	s_cbranch_scc1 .LBB0_1934
	v_readlane_b32 s0, v255, 0
	v_readlane_b32 s1, v255, 1
	v_mov_b32_e32 v1, v0
	s_lshl_b32 s2, s97, 3
	v_readfirstlane_b32 s3, v1
	s_ashr_i32 s3, s3, 6
	s_add_i32 s6, s3, s2
	s_cmpk_gt_i32 s6, 0x1fff
	s_cbranch_scc1 .LBB0_1934
	s_mov_b64 s[4:5], s[98:99]
	s_load_dwordx2 s[2:3], s[0:1], 0x38
	s_load_dwordx2 s[10:11], s[0:1], 0x48
	s_load_dwordx2 s[12:13], s[0:1], 0x60
	v_and_b32_e32 v6, 1, v1
	v_and_b32_e32 v8, 63, v1
	v_mov_b32_e32 v3, 0
	v_cmp_eq_u32_e64 s[0:1], 0, v6
	v_lshlrev_b32_e32 v6, 2, v1
	v_lshlrev_b32_e32 v2, 5, v8
	v_and_b32_e32 v54, 60, v6
	v_lshlrev_b32_e32 v6, 6, v8
	v_mov_b32_e32 v7, v3
	s_waitcnt lgkmcnt(0)
	v_lshl_add_u64 v[50:51], s[2:3], 0, v[2:3]
	v_lshl_add_u64 v[6:7], s[12:13], 0, v[6:7]
	s_mov_b64 s[2:3], 0x3000
	s_add_u32 s8, s4, 0x200000
	v_lshl_add_u64 v[56:57], v[6:7], 0, s[2:3]
	s_mov_b64 s[2:3], 0x4000
	s_addc_u32 s9, s5, 0
	v_lshl_add_u64 v[58:59], v[6:7], 0, s[2:3]
	s_mov_b64 s[2:3], 0x5000
	s_ashr_i32 s7, s6, 31
	v_lshl_add_u64 v[60:61], v[6:7], 0, s[2:3]
	s_lshl_b64 s[2:3], s[6:7], 11
	v_lshlrev_b32_e32 v9, 3, v8
	v_or_b32_e32 v64, s2, v2
	v_mov_b32_e32 v65, s3
	s_lshl_b64 s[2:3], s[6:7], 9
	v_lshlrev_b32_e32 v4, 4, v8
	v_mov_b32_e32 v5, v3
	v_or_b32_e32 v66, s2, v9
	v_mov_b32_e32 v67, s3
	s_lshl_b64 s[2:3], s[6:7], 14
	v_lshl_add_u64 v[52:53], s[10:11], 0, v[4:5]
	v_mov_b32_e32 v55, v3
	v_or_b32_e32 v68, s2, v2
	v_or_b32_e32 v2, s2, v9
	v_mov_b32_e32 v3, s3
	s_mov_b64 s[10:11], 0x3e400400
	v_lshl_add_u64 v[70:71], v[2:3], 0, s[10:11]
	v_lshl_or_b32 v2, v8, 1, s2
	s_mov_b64 s[10:11], 0x3e400600
	v_mov_b32_e32 v69, s3
	v_lshl_add_u64 v[72:73], v[2:3], 0, s[10:11]
	v_or_b32_e32 v2, s2, v4
	s_mov_b64 s[2:3], 0x3e400000
	v_lshl_add_u64 v[74:75], v[2:3], 0, s[2:3]
	v_mbcnt_lo_u32_b32 v2, -1, 0
	v_mbcnt_hi_u32_b32 v97, -1, v2
	v_and_b32_e32 v2, 64, v97
	v_bfe_u32 v5, v1, 1, 5
	v_add_u32_e32 v99, 64, v2
	v_or_b32_e32 v2, v2, v54
	v_bfe_u32 v1, v1, 4, 2
	v_lshl_or_b32 v62, s6, 5, v5
	v_mov_b32_e32 v96, 0x358637bd
	s_mov_b32 s7, 0x800000
	s_mov_b32 s30, 0x46400000
	s_mov_b32 s31, 0x46c00000
	s_movk_i32 s33, 0xc0
	s_mov_b32 s34, 0x4b000000
	s_mov_b32 s35, 0x4b300000
	s_mov_b64 s[10:11], 0x3e3fd000
	s_mov_b64 s[12:13], 0x3e3fd800
	s_mov_b64 s[14:15], 0x3e401000
	s_mov_b64 s[16:17], 0x3e401800
	s_mov_b64 s[18:19], 0x3e405000
	s_mov_b64 s[20:21], 0x3e405800
	s_mov_b64 s[22:23], 0x3e400800
	s_mov_b32 s36, 0x3e400000
	s_mov_b32 s37, 0x47000000
	s_mov_b64 s[24:25], 0x400000
	s_mov_b64 s[26:27], 0x100000
	s_mov_b64 s[28:29], 0x2000000
	v_xor_b32_e32 v98, 1, v97
	v_lshlrev_b32_e32 v100, 2, v2
	v_mov_b64_e32 v[76:77], s[4:5]
	global_load_dwordx4 v[170:173], v[56:57], off offset:16
	global_load_dwordx4 v[174:177], v[56:57], off
	global_load_dwordx4 v[178:181], v[58:59], off offset:16
	global_load_dwordx4 v[182:185], v[58:59], off
	global_load_dwordx4 v[186:189], v[60:61], off offset:16
	global_load_dwordx4 v[190:193], v[60:61], off
	global_load_dwordx4 v[194:197], v[56:57], off offset:48
	global_load_dwordx4 v[198:201], v[56:57], off offset:32
	global_load_dwordx4 v[202:205], v[58:59], off offset:48
	global_load_dwordx4 v[206:209], v[58:59], off offset:32
	global_load_dwordx4 v[210:213], v[60:61], off offset:48
	global_load_dwordx4 v[214:217], v[60:61], off offset:32
	s_branch .LBB0_1927

; __device__ __forceinline__ float bflo(unsigned w) { return __uint_as_float(w << 16); }
; __device__ __forceinline__ void postproj_phase(CArgs& A, int l, int vcu, int G) {
;     ...
;     for (int t = vcu * NWAVES + wave; t < NT; t += G * NWAVES) {
;         const int b = t / SEQ, s = t % SEQ; const bf16* pr = P + (size_t)t * NINP;
;         {
;             const u32x4 w = *(const u32x4*)(pr + PC_CQ + 8 * lane); float v[8] = {bflo(w.x), bfhi(w.x), bflo(w.y), bfhi(w.y), bflo(w.z), bfhi(w.z), bflo(w.w), bfhi(w.w)};
;             float ss = 0.f;
; #pragma unroll
;             for (int q = 0; q < 8; ++q) ss += v[q] * v[q];
;             const float rstd = rsqrtf(wave_sum(ss) * (1.0f / QL) + EPS);
;             const f32x4 g0 = *(const f32x4*)(gq + 8 * lane), g1 = *(const f32x4*)(gq + 8 * lane + 4);
;             u32x4 o; o.x = cvtpk(v[0] * rstd * g0.x, v[1] * rstd * g0.y); o.y = cvtpk(v[2] * rstd * g0.z, v[3] * rstd * g0.w); o.z = cvtpk(v[4] * rstd * g1.x, v[5] * rstd * g1.y); o.w = cvtpk(v[6] * rstd * g1.z, v[7] * rstd * g1.w);
;             *(u32x2*)((unsigned char*)CQN + (size_t)t * QL + 8 * lane) = pack8_fp8((f32x4){v[0] * rstd * g0.x, v[1] * rstd * g0.y, v[2] * rstd * g0.z, v[3] * rstd * g0.w}, (f32x4){v[4] * rstd * g1.x, v[5] * rstd * g1.y, v[6] * rstd * g1.z, v[7] * rstd * g1.w});
;         }
;         {
;             const u32x2 w = *(const u32x2*)(pr + PC_CKV + 4 * lane); float v[4] = {bflo(w.x), bfhi(w.x), bflo(w.y), bfhi(w.y)};
;             const float rstd = rsqrtf(wave_sum(v[0] * v[0] + v[1] * v[1] + v[2] * v[2] + v[3] * v[3]) * (1.0f / KVL) + EPS);
;             const f32x4 g0 = *(const f32x4*)(gkv + 4 * lane);
;             u32x2 o; o.x = cvtpk(v[0] * rstd * g0.x, v[1] * rstd * g0.y); o.y = cvtpk(v[2] * rstd * g0.z, v[3] * rstd * g0.w);
;             *(u32x2*)(CKVN + (size_t)t * KVL + 4 * lane) = o;
;         }
;         {
;             const float v = __uint_as_float((unsigned)pr[PC_KPE + lane] << 16); const float o = __shfl_xor(v, 1);
;             const f32x2 c = cs[t * 32 + (lane >> 1)];
;             const float r = ((lane & 1) ? (v * c.x + o * c.y) : (v * c.x - o * c.y)) * 0.25f;
;             const int w1 = __builtin_amdgcn_cvt_pk_fp8_f32(r, r, 0, false) & 0xff;
;             const unsigned q0 = (unsigned)__builtin_amdgcn_update_dpp(0, w1, 0x00, 0xf, 0xf, true), q1 = (unsigned)__builtin_amdgcn_update_dpp(0, w1, 0x55, 0xf, 0xf, true);
.LBB0_1927:
	v_lshl_add_u64 v[14:15], s[4:5], 0, v[74:75]
	global_load_dwordx4 v[2:5], v[14:15], off
	global_load_dwordx4 v[6:9], v[50:51], off offset:2048
	global_load_dwordx4 v[10:13], v[50:51], off offset:2064
	v_mov_b32_e32 v14, 0
	v_mov_b32_e32 v15, 0
	v_lshl_add_u64 v[16:17], s[4:5], 0, v[66:67]
	v_lshl_add_u64 v[18:19], s[4:5], 0, v[70:71]
	v_ashrrev_i32_e32 v63, 31, v62
	v_lshl_add_u64 v[78:79], s[4:5], 0, v[68:69]
	global_load_dwordx2 v[142:143], v[18:19], off
	global_load_dwordx4 v[144:147], v[52:53], off offset:1024
	v_lshl_add_u64 v[148:149], s[4:5], 0, v[72:73]
	global_load_ushort v150, v[148:149], off
	v_lshl_add_u64 v[152:153], v[62:63], 3, s[8:9]
	global_load_dwordx2 v[154:155], v[152:153], off
	v_mov_b32_e32 v158, s36
	v_mov_b32_e32 v159, 0
	v_lshl_add_u64 v[156:157], v[78:79], 0, v[158:159]
	global_load_dwordx4 v[160:163], v[156:157], off offset:2048
	v_lshl_add_u64 v[164:165], v[78:79], 0, s[22:23]
	global_load_dwordx4 v[166:169], v[164:165], off offset:16
	s_waitcnt vmcnt(0)
	v_and_b32_e32 v29, 0xffff0000, v2
	v_lshlrev_b32_e32 v28, 16, v2
	v_and_b32_e32 v2, 0xffff0000, v3
	v_lshlrev_b32_e32 v3, 16, v3
	v_mul_f32_e32 v30, v29, v29
	v_pk_mul_f32 v[22:23], v[2:3], v[2:3]
	v_fmac_f32_e32 v30, v28, v28
	v_and_b32_e32 v20, 0xffff0000, v4
	v_lshlrev_b32_e32 v21, 16, v4
	v_add_f32_e32 v23, v23, v30
	v_pk_mul_f32 v[24:25], v[20:21], v[20:21]
	v_add_f32_e32 v22, v22, v23
	v_and_b32_e32 v4, 0xffff0000, v5
	v_lshlrev_b32_e32 v5, 16, v5
	v_add_f32_e32 v22, v25, v22
	v_pk_mul_f32 v[26:27], v[4:5], v[4:5]
	v_add_f32_e32 v22, v24, v22
	v_add_f32_e32 v22, v27, v22
	v_add_f32_e32 v22, v26, v22
	s_nop 1
	v_add_f32_dpp v22, v22, v22 quad_perm:[1,0,3,2] row_mask:0xf bank_mask:0xf bound_ctrl:1
	s_nop 1
	v_add_f32_dpp v22, v22, v22 quad_perm:[2,3,0,1] row_mask:0xf bank_mask:0xf bound_ctrl:1
	s_nop 1
	v_add_f32_dpp v22, v22, v22 row_half_mirror row_mask:0xf bank_mask:0xf bound_ctrl:1
	s_nop 1
	v_add_f32_dpp v22, v22, v22 row_mirror row_mask:0xf bank_mask:0xf bound_ctrl:1
	s_nop 0
	v_readlane_b32 s38, v22, 16
	v_readlane_b32 s39, v22, 48
	v_readlane_b32 s2, v22, 0
	v_readlane_b32 s3, v22, 32
	v_mov_b32_e32 v22, s38
	v_mov_b32_e32 v23, s39
	v_pk_add_f32 v[22:23], s[2:3], v[22:23]
	s_nop 0
	v_add_f32_e32 v22, v22, v23
	v_fmamk_f32 v22, v22, 0x3b000000, v96
	v_mul_f32_e32 v23, 0x4b800000, v22
	v_cmp_gt_f32_e32 vcc, s7, v22
	s_nop 1
	v_cndmask_b32_e32 v22, v22, v23, vcc
	v_rsq_f32_e32 v24, v22
	v_add_co_u32_e64 v22, s[2:3], s30, v16
	v_mul_f32_e32 v25, 0x45800000, v24
	v_cndmask_b32_e32 v24, v24, v25, vcc
	v_mul_f32_e32 v25, v24, v28
	v_mul_f32_e32 v26, v24, v29
	v_mul_f32_e32 v3, v24, v3
	v_mul_f32_e32 v2, v24, v2
	v_mul_f32_e32 v21, v24, v21
	v_mul_f32_e32 v20, v24, v20
	v_mul_f32_e32 v6, v6, v25
	v_mul_f32_e32 v7, v7, v26
	v_mul_f32_e32 v3, v8, v3
	v_mul_f32_e32 v2, v9, v2
	v_mul_f32_e32 v8, v10, v21
	v_mul_f32_e32 v9, v11, v20
	v_cvt_pk_fp8_f32 v14, v6, v7
	v_cvt_pk_fp8_f32 v15, v8, v9
	v_mul_f32_e32 v5, v24, v5
	v_mul_f32_e32 v4, v24, v4
	v_mul_f32_e32 v5, v12, v5
	v_mul_f32_e32 v4, v13, v4
	v_cvt_pk_fp8_f32 v14, v3, v2 op_sel:[0,0,1]
	v_cvt_pk_fp8_f32 v15, v5, v4 op_sel:[0,0,1]
	v_addc_co_u32_e64 v23, s[2:3], 0, v17, s[2:3]
	v_cvt_pk_bf16_f32 v6, v6, v7
	v_cvt_pk_bf16_f32 v2, v3, v2
	v_mov_b32_e32 v28, 0
	v_cvt_pk_bf16_f32 v2, v8, v9
	v_lshl_add_u64 v[8:9], s[4:5], 0, v[72:73]
	v_cvt_pk_bf16_f32 v2, v5, v4
	global_store_dwordx2 v[22:23], v[14:15], off
	v_mov_b32_e32 v6, v142
	v_mov_b32_e32 v7, v143
	v_mov_b32_e32 v2, v144
	v_mov_b32_e32 v3, v145
	v_mov_b32_e32 v4, v146
	v_mov_b32_e32 v5, v147
	v_lshlrev_b32_e32 v10, 16, v6
	v_and_b32_e32 v11, 0xffff0000, v6
	v_and_b32_e32 v6, 0xffff0000, v7
	v_lshlrev_b32_e32 v7, 16, v7
	v_pk_mul_f32 v[12:13], v[10:11], v[10:11]
	v_pk_mul_f32 v[14:15], v[6:7], v[6:7]
	v_add_f32_e32 v12, v12, v13
	v_add_f32_e32 v12, v15, v12
	v_add_f32_e32 v12, v14, v12
	s_nop 1
	v_add_f32_dpp v12, v12, v12 quad_perm:[1,0,3,2] row_mask:0xf bank_mask:0xf bound_ctrl:1
	s_nop 1
	v_add_f32_dpp v12, v12, v12 quad_perm:[2,3,0,1] row_mask:0xf bank_mask:0xf bound_ctrl:1
	s_nop 1
	v_add_f32_dpp v12, v12, v12 row_half_mirror row_mask:0xf bank_mask:0xf bound_ctrl:1
	s_nop 1
	v_add_f32_dpp v12, v12, v12 row_mirror row_mask:0xf bank_mask:0xf bound_ctrl:1
	s_nop 0
	v_readlane_b32 s38, v12, 16
	v_readlane_b32 s39, v12, 48
	v_readlane_b32 s2, v12, 0
	v_readlane_b32 s3, v12, 32
	v_mov_b32_e32 v12, s38
	v_mov_b32_e32 v13, s39
	v_pk_add_f32 v[12:13], s[2:3], v[12:13]
	s_nop 0
	v_add_f32_e32 v12, v12, v13
	v_fmamk_f32 v12, v12, 0x3b800000, v96
	v_mul_f32_e32 v13, 0x4b800000, v12
	v_cmp_gt_f32_e32 vcc, s7, v12
	s_nop 1
	v_cndmask_b32_e32 v12, v12, v13, vcc
	v_rsq_f32_e32 v14, v12
	v_add_co_u32_e64 v12, s[2:3], s31, v16
	v_mov_b32_e32 v16, 0
	v_mul_f32_e32 v15, 0x45800000, v14
	v_cndmask_b32_e32 v14, v14, v15, vcc
	v_mul_f32_e32 v10, v14, v10
	v_mul_f32_e32 v11, v14, v11
	v_addc_co_u32_e64 v13, s[2:3], 0, v17, s[2:3]
	v_mul_f32_e32 v7, v14, v7
	v_mul_f32_e32 v6, v14, v6
	v_mul_f32_e32 v2, v2, v10
	v_mul_f32_e32 v3, v3, v11
	v_mul_f32_e32 v4, v4, v7
	v_mul_f32_e32 v5, v5, v6
	v_cvt_pk_bf16_f32 v2, v2, v3
	v_cvt_pk_bf16_f32 v3, v4, v5
	global_store_dwordx2 v[12:13], v[2:3], off
	v_mov_b32_e32 v9, v150
	v_lshl_add_u64 v[2:3], v[62:63], 3, s[8:9]
	v_mov_b32_e32 v18, v154
	v_mov_b32_e32 v19, v155
	v_cmp_lt_i32_e32 vcc, v98, v99
	s_ashr_i32 s2, s6, 31
	s_lshr_b32 s2, s2, 20
	v_cndmask_b32_e32 v20, v97, v98, vcc
	v_lshlrev_b32_e32 v25, 2, v20
	s_add_i32 s2, s6, s2
	s_ashr_i32 s3, s2, 12
	s_and_b32 s2, s2, 0xfffff000
	v_lshl_or_b32 v20, s3, 4, v1
	s_sub_i32 s2, s6, s2
	v_ashrrev_i32_e32 v21, 31, v20
	s_ashr_i32 s3, s2, 31
	v_lshlrev_b64 v[20:21], 12, v[20:21]
	s_add_i32 s38, s2, -1
	v_lshl_add_u64 v[20:21], v[20:21], 0, s[2:3]
	s_cmpk_gt_u32 s38, 0xfff
	v_mad_u64_u32 v[22:23], s[38:39], v20, s33, v[76:77]
	v_mad_i32_i24 v23, v21, s33, v23
	v_lshl_add_u64 v[20:21], v[22:23], 0, v[54:55]
	v_add_co_u32_e32 v22, vcc, s34, v20
	v_mov_b32_e32 v10, 0
	s_nop 0
	v_addc_co_u32_e32 v23, vcc, 0, v21, vcc
	v_add_co_u32_e32 v24, vcc, s35, v20
	v_mov_b32_e32 v11, 0
	v_mov_b32_e32 v12, 0
	v_mov_b32_e32 v13, 0
	v_mov_b32_e32 v2, 0
	v_mov_b32_e32 v3, 0
	v_mov_b32_e32 v4, 0
	v_mov_b32_e32 v5, 0
	v_mov_b32_e32 v14, 0
	v_mov_b32_e32 v15, 0
	v_mov_b32_e32 v17, 0
	v_mov_b32_e32 v6, 0
	v_mov_b32_e32 v7, 0
	v_mov_b32_e32 v8, 0
	v_lshlrev_b32_e32 v9, 16, v9
	ds_bpermute_b32 v27, v25, v9
	v_addc_co_u32_e32 v25, vcc, 0, v21, vcc
	v_add_co_u32_e32 v26, vcc, 0x4b600000, v20
	s_waitcnt lgkmcnt(0)
; __device__ __forceinline__ void postproj_phase(CArgs& A, int l, int vcu, int G) {
;     ...
;             const float v = __uint_as_float((unsigned)pr[PC_KPE + lane] << 16); const float o = __shfl_xor(v, 1);
;             const f32x2 c = cs[t * 32 + (lane >> 1)];
;             const float r = ((lane & 1) ? (v * c.x + o * c.y) : (v * c.x - o * c.y)) * 0.25f;
;             const int w1 = __builtin_amdgcn_cvt_pk_fp8_f32(r, r, 0, false) & 0xff;
;             const unsigned q0 = (unsigned)__builtin_amdgcn_update_dpp(0, w1, 0x00, 0xf, 0xf, true), q1 = (unsigned)__builtin_amdgcn_update_dpp(0, w1, 0x55, 0xf, 0xf, true);
;             const unsigned q2 = (unsigned)__builtin_amdgcn_update_dpp(0, w1, 0xAA, 0xf, 0xf, true), q3 = (unsigned)__builtin_amdgcn_update_dpp(0, w1, 0xFF, 0xf, 0xf, true);
;             const unsigned wq = q0 | (q1 << 8) | (q2 << 16) | (q3 << 24);
;             const unsigned wg = (unsigned)__shfl((int)wq, 4 * (lane & 15));
;             unsigned char* kd = Kb + ((size_t)(b * NH + (lane >> 4)) * SEQ + s) * DQK + DNOPE + 4 * (lane & 15);
; #pragma unroll
;             for (int hg = 0; hg < 4; ++hg) *(unsigned*)(kd + (size_t)(4 * hg) * SEQ * DQK) = wg;
;         }
;         {
;             const int c0 = 16 * lane;
;             float z[3][16];
; #pragma unroll
;             for (int d = 0; d < 3; ++d) {
;                 const int ss = s + d - 1; const bool ok = (ss >= 0 && ss < SEQ);
;                 const bf16* p2 = pr + (ptrdiff_t)(d - 1) * NINP;
;                 u32x4 gc0 = {0, 0, 0, 0}, gc1 = gc0, u0 = gc0, u1 = gc0;
;                 if (ok) { gc0 = *(const u32x4*)(p2 + PC_GC + c0); gc1 = *(const u32x4*)(p2 + PC_GC + c0 + 8); u0 = *(const u32x4*)(p2 + PC_U + c0); u1 = *(const u32x4*)(p2 + PC_U + c0 + 8); }
	v_mul_f32_e32 v19, v19, v27
	v_cndmask_b32_e64 v19, v19, -v19, s[0:1]
	v_fmac_f32_e32 v19, v18, v9
	v_mul_f32_e32 v9, 0x3e800000, v19
	v_cvt_pk_fp8_f32 v28, v9, v9
	v_addc_co_u32_e32 v27, vcc, 0, v21, vcc
	v_and_b32_e32 v9, 0xff, v28
	s_nop 1
	v_mov_b32_dpp v18, v9 quad_perm:[0,0,0,0] row_mask:0xf bank_mask:0xf bound_ctrl:1
	v_mov_b32_dpp v19, v9 quad_perm:[1,1,1,1] row_mask:0xf bank_mask:0xf bound_ctrl:1
	v_mov_b32_dpp v28, v9 quad_perm:[2,2,2,2] row_mask:0xf bank_mask:0xf bound_ctrl:1
	v_mov_b32_dpp v9, v9 quad_perm:[3,3,3,3] row_mask:0xf bank_mask:0xf bound_ctrl:1
	v_lshl_or_b32 v18, v19, 8, v18
	v_lshlrev_b32_e32 v19, 16, v28
	v_lshlrev_b32_e32 v9, 24, v9
	v_or3_b32 v9, v18, v19, v9
	ds_bpermute_b32 v9, v100, v9
	v_add_co_u32_e32 v18, vcc, 0x4b900000, v20
	s_nop 1
	v_addc_co_u32_e32 v19, vcc, 0, v21, vcc
	s_waitcnt lgkmcnt(0)
	global_store_dword v[22:23], v9, off offset:128
	global_store_dword v[24:25], v9, off offset:128
	global_store_dword v[26:27], v9, off offset:128
	global_store_dword v[18:19], v9, off offset:128
	v_mov_b32_e32 v9, 0
	s_cbranch_scc1 .LBB0_1929
	v_add_co_u32_e32 v18, vcc, 0x3e3fd000, v78
	v_lshl_add_u64 v[6:7], v[78:79], 0, s[10:11]
	s_nop 0
	v_addc_co_u32_e32 v19, vcc, 0, v79, vcc
	global_load_dwordx4 v[10:13], v[18:19], off
	global_load_dwordx4 v[2:5], v[6:7], off offset:16
	v_lshl_add_u64 v[20:21], v[78:79], 0, s[12:13]
	global_load_dwordx4 v[14:17], v[18:19], off offset:2048
	global_load_dwordx4 v[6:9], v[20:21], off offset:16
